# sel QK: first scale MFMA issued after the first two K reads, first eight V^T reads moved into its shadow, counted lgkmcnt 12/10/8
# speedup vs baseline: 1.0264x; 1.0008x over previous
; __device__ __forceinline__ unsigned lds_addr(const LAS void* p) { return (unsigned)(size_t)p; }
; #define RD16(dst, base, off) asm volatile("ds_read_b128 %0, %1 offset:%2" : "=&v"(dst) : "v"(base), "i"(off) : "memory")
; #define LGKM_W(n) asm volatile("s_waitcnt lgkmcnt(" #n ")" ::: "memory"); SBAR()
; #define QK8_MM(T_) do { i32x8a kf; kf.lo = lo[T_]; kf.hi = hi[T_]; s[T_] = __builtin_amdgcn_mfma_scale_f32_16x16x128_f8f6f4(kf, g.q8, (f32x4){c0, c0, c0, c0}, 0, 0, 0, 0x7f7f7f7f, 0, 0x7c7c7c7c); } while (0)
; #define PV8_RD(dt) do { RD8(f.a[dt][0], vb, (dt) * 16 * VT8ST); RD8(f.a[dt][1], vb, (dt) * 16 * VT8ST + 32); } while (0)
; __device__ __forceinline__ void qk8_tile_c(f32x4 (&s)[4], const GS8& g, const unsigned kb  , const float c0  ) {
;     i32x4a lo[4], hi[4];
;     RD16(lo[0], kb, 0); RD16(hi[0], kb, 16); RD16(lo[1], kb, 16 * K8ST); RD16(hi[1], kb, 16 * K8ST + 16);
;     RD16(lo[2], kb, 32 * K8ST); RD16(hi[2], kb, 32 * K8ST + 16); RD16(lo[3], kb, 48 * K8ST); RD16(hi[3], kb, 48 * K8ST + 16);
;     ...
;     LGKM_W(6); QK8_MM(0); LGKM_W(4); QK8_MM(1); LGKM_W(2); QK8_MM(2); LGKM_W(0); QK8_MM(3);
;     ...
; }
; __device__ __forceinline__ void pv8_issue(VT8Frag& f, const unsigned vb  ) {
;     ...
;     PV8_RD(0); PV8_RD(1); PV8_RD(2); PV8_RD(3); PV8_RD(4); PV8_RD(5); PV8_RD(6); PV8_RD(7);
;     ...
; }
; template <bool DUMMY> __device__ __forceinline__ void sel_phase(Frame& F) {
;     ...
;                 const unsigned a0 = byte & 0xfu, a1 = byte >> 4;
;                 if (byte == 0u) continue;
;                 const bool selA = ((a0 >> (c >> 2)) & 1u) != 0u, selB = ((a1 >> (c >> 2)) & 1u) != 0u;
;                 const float NINF = -__builtin_inff();
;                 const int kb = jc * 64; const bool diag = (jc == cur); f32x4 s0[4], s1[4];
;                 const float bA = selA ? 0.f : NINF, bB = selB ? 0.f : NINF;
;                 if (a0 != 0u) {
;                     const float rf = sm8_ref(g0);
;                     VT8Frag vf; qk8_tile_c(s0, g0, lds_addr(sb) + (unsigned)klane, bA + (5.f - rf)); pv8_issue(vf, lds_addr(sb + K8TB) + (unsigned)vtlane);
;                     if (diag) mask_scores(s0, tokA, 0x40000000u, kb, kq);
.LBB0_1801:
	s_andn2_b64 vcc, exec, s[12:13]
	s_cbranch_vccnz .LBB0_1798
	s_lshr_b32 s45, s67, s36
	s_and_b32 s97, s45, 0xff
	s_cmp_eq_u32 s97, 0
	s_cbranch_scc1 .LBB0_1798
	s_lshr_b32 s12, s66, s36
	s_and_b32 s12, s12, 0xff
	s_and_b32 vcc_lo, s45, 15
	s_lshl_b32 s44, s12, 6
	s_cmp_eq_u32 s12, s58
	s_cselect_b64 s[12:13], -1, 0
	v_cndmask_b32_e64 v18, 0, 1, s[12:13]
	s_cmp_eq_u32 vcc_lo, 0
	v_cmp_ne_u32_e64 s[12:13], 1, v18
	s_cbranch_scc1 .LBB0_1809
	ds_read_b128 v[84:87], v208 offset:0
	ds_read_b128 v[88:91], v208 offset:16
	ds_read_b128 v[92:95], v208 offset:0x900
	ds_read_b128 v[96:99], v208 offset:0x910
	ds_read_b128 v[118:121], v208 offset:0x1200
	ds_read_b128 v[122:125], v208 offset:0x1210
	ds_read_b128 v[126:129], v208 offset:0x1b00
	ds_read_b128 v[130:133], v208 offset:0x1b10
	v_and_b32_e32 v18, s45, v154
	v_cmp_eq_u32_e32 vcc, 0, v18
	s_nop 1
	v_cndmask_b32_e32 v18, 0, v181, vcc
	v_cmp_ngt_f32_e32 vcc, s90, v19
	s_nop 1
	v_cndmask_b32_e32 v116, 0, v19, vcc
	v_sub_f32_e32 v114, 0x40a00000, v116
	v_add_f32_e32 v210, v114, v18
	v_mov_b32_e32 v211, v210
	v_mov_b32_e32 v212, v210
	v_mov_b32_e32 v213, v210
	s_waitcnt lgkmcnt(6)
	s_nop 1
	v_mfma_scale_f32_16x16x128_f8f6f4 v[84:87], v[84:91], v[0:7], v[210:213], v178, v177 op_sel_hi:[0,0,0]
	ds_read_b64 v[148:149], v207 offset:0
	ds_read_b64 v[146:147], v207 offset:32
	ds_read_b64 v[144:145], v207 offset:0x500
	ds_read_b64 v[142:143], v207 offset:0x520
	ds_read_b64 v[140:141], v207 offset:0xa00
	ds_read_b64 v[136:137], v207 offset:0xa20
	ds_read_b64 v[138:139], v207 offset:0xf00
	ds_read_b64 v[134:135], v207 offset:0xf20
	s_waitcnt lgkmcnt(12)
	v_mfma_scale_f32_16x16x128_f8f6f4 v[88:91], v[92:99], v[0:7], v[210:213], v178, v177 op_sel_hi:[0,0,0]
	s_waitcnt lgkmcnt(10)
	v_mfma_scale_f32_16x16x128_f8f6f4 v[92:95], v[118:125], v[0:7], v[210:213], v178, v177 op_sel_hi:[0,0,0]
	s_waitcnt lgkmcnt(8)
	v_mfma_scale_f32_16x16x128_f8f6f4 v[96:99], v[126:133], v[0:7], v[210:213], v178, v177 op_sel_hi:[0,0,0]
	ds_read_b64 v[132:133], v207 offset:0x1400
	ds_read_b64 v[130:131], v207 offset:0x1420
	ds_read_b64 v[128:129], v207 offset:0x1900
	ds_read_b64 v[126:127], v207 offset:0x1920
	ds_read_b64 v[124:125], v207 offset:0x1e00
	ds_read_b64 v[120:121], v207 offset:0x1e20
	ds_read_b64 v[118:119], v207 offset:0x2300
	ds_read_b64 v[122:123], v207 offset:0x2320
	s_and_b64 vcc, exec, s[12:13]
	s_cbranch_vccnz .LBB0_1806
	v_add_u32_e32 v18, s44, v155
	v_sub_u32_e32 v114, s55, v18
	v_cmp_gt_u32_e32 vcc, 2.0, v114
	v_sub_u32_e32 v114, v18, v16
	s_nop 2
	v_cndmask_b32_e32 v84, v181, v84, vcc
	v_cmp_lt_u32_e32 vcc, s91, v114
	v_sub_u32_e32 v114, v184, v18
	s_nop 0
	v_cndmask_b32_e32 v85, v181, v85, vcc
	v_cmp_gt_u32_e32 vcc, 2.0, v114
	v_sub_u32_e32 v114, v185, v18
	s_nop 0
	v_cndmask_b32_e32 v86, v181, v86, vcc
	v_cmp_gt_u32_e32 vcc, 2.0, v114
	v_sub_u32_e32 v114, s68, v18
	s_nop 0
	v_cndmask_b32_e32 v87, v181, v87, vcc
	v_cmp_gt_u32_e32 vcc, 2.0, v114
	v_sub_u32_e32 v114, v186, v18
	s_nop 0
	v_cndmask_b32_e32 v88, v181, v88, vcc
	v_cmp_gt_u32_e32 vcc, 2.0, v114
	v_sub_u32_e32 v114, v187, v18
	s_nop 0
	v_cndmask_b32_e32 v89, v181, v89, vcc
	v_cmp_gt_u32_e32 vcc, 2.0, v114
	v_sub_u32_e32 v114, v188, v18
	s_nop 0
	v_cndmask_b32_e32 v90, v181, v90, vcc
	v_cmp_gt_u32_e32 vcc, 2.0, v114
	v_sub_u32_e32 v114, s69, v18
	s_nop 0
	v_cndmask_b32_e32 v91, v181, v91, vcc
	v_cmp_gt_u32_e32 vcc, 2.0, v114
	v_sub_u32_e32 v114, v189, v18
	s_nop 0
	v_cndmask_b32_e32 v92, v181, v92, vcc
	v_cmp_gt_u32_e32 vcc, 2.0, v114
	v_sub_u32_e32 v114, v190, v18
	s_nop 0
	v_cndmask_b32_e32 v93, v181, v93, vcc
	v_cmp_gt_u32_e32 vcc, 2.0, v114
	v_sub_u32_e32 v114, v191, v18
	s_nop 0
	v_cndmask_b32_e32 v94, v181, v94, vcc
	v_cmp_gt_u32_e32 vcc, 2.0, v114
	v_sub_u32_e32 v114, s70, v18
	s_nop 0
	v_cndmask_b32_e32 v95, v181, v95, vcc
	v_cmp_gt_u32_e32 vcc, 2.0, v114
	v_sub_u32_e32 v114, v192, v18
	s_nop 0
	v_cndmask_b32_e32 v96, v181, v96, vcc
	v_cmp_gt_u32_e32 vcc, 2.0, v114
	v_sub_u32_e32 v114, v193, v18
	v_sub_u32_e32 v18, v194, v18
	v_cndmask_b32_e32 v97, v181, v97, vcc
	v_cmp_gt_u32_e32 vcc, 2.0, v114
	s_nop 1
	v_cndmask_b32_e32 v98, v181, v98, vcc
	v_cmp_gt_u32_e32 vcc, 2.0, v18
	s_nop 1
	v_cndmask_b32_e32 v99, v181, v99, vcc

; __device__ __forceinline__ unsigned lds_addr(const LAS void* p) { return (unsigned)(size_t)p; }
; #define RD16(dst, base, off) asm volatile("ds_read_b128 %0, %1 offset:%2" : "=&v"(dst) : "v"(base), "i"(off) : "memory")
; #define LGKM_W(n) asm volatile("s_waitcnt lgkmcnt(" #n ")" ::: "memory"); SBAR()
; #define QK8_MM(T_) do { i32x8a kf; kf.lo = lo[T_]; kf.hi = hi[T_]; s[T_] = __builtin_amdgcn_mfma_scale_f32_16x16x128_f8f6f4(kf, g.q8, (f32x4){c0, c0, c0, c0}, 0, 0, 0, 0x7f7f7f7f, 0, 0x7c7c7c7c); } while (0)
; #define PV8_RD(dt) do { RD8(f.a[dt][0], vb, (dt) * 16 * VT8ST); RD8(f.a[dt][1], vb, (dt) * 16 * VT8ST + 32); } while (0)
; __device__ __forceinline__ void qk8_tile_c(f32x4 (&s)[4], const GS8& g, const unsigned kb  , const float c0  ) {
;     i32x4a lo[4], hi[4];
;     RD16(lo[0], kb, 0); RD16(hi[0], kb, 16); RD16(lo[1], kb, 16 * K8ST); RD16(hi[1], kb, 16 * K8ST + 16);
;     RD16(lo[2], kb, 32 * K8ST); RD16(hi[2], kb, 32 * K8ST + 16); RD16(lo[3], kb, 48 * K8ST); RD16(hi[3], kb, 48 * K8ST + 16);
;     ...
;     LGKM_W(6); QK8_MM(0); LGKM_W(4); QK8_MM(1); LGKM_W(2); QK8_MM(2); LGKM_W(0); QK8_MM(3);
;     ...
; }
; __device__ __forceinline__ void pv8_issue(VT8Frag& f, const unsigned vb  ) {
;     ...
;     PV8_RD(0); PV8_RD(1); PV8_RD(2); PV8_RD(3); PV8_RD(4); PV8_RD(5); PV8_RD(6); PV8_RD(7);
;     ...
; }
; template <bool DUMMY> __device__ __forceinline__ void sel_phase(Frame& F) {
;     ...
;                 if (a1 != 0u) {
;                     const float rf = sm8_ref(g1);
;                     VT8Frag vf; qk8_tile_c(s0, g1, lds_addr(sb) + (unsigned)klane, bB + (5.f - rf)); pv8_issue(vf, lds_addr(sb + K8TB) + (unsigned)vtlane);
;                     if (diag) mask_scores(s0, tokA + 4, 0x40000000u, kb, kq);
.LBB0_1809:
	s_cmp_lt_u32 s97, 16
	s_cbranch_scc1 .LBB0_1798
	s_lshr_b32 s45, s45, 4
	ds_read_b128 v[84:87], v208 offset:0
	ds_read_b128 v[88:91], v208 offset:16
	ds_read_b128 v[92:95], v208 offset:0x900
	ds_read_b128 v[96:99], v208 offset:0x910
	ds_read_b128 v[118:121], v208 offset:0x1200
	ds_read_b128 v[122:125], v208 offset:0x1210
	ds_read_b128 v[126:129], v208 offset:0x1b00
	ds_read_b128 v[130:133], v208 offset:0x1b10
	v_and_b32_e32 v18, s45, v154
	v_cmp_eq_u32_e32 vcc, 0, v18
	s_nop 1
	v_cndmask_b32_e32 v114, 0, v181, vcc
	v_cmp_ngt_f32_e32 vcc, s90, v117
	s_nop 1
	v_cndmask_b32_e32 v18, 0, v117, vcc
	v_sub_f32_e32 v116, 0x40a00000, v18
	v_add_f32_e32 v210, v114, v116
	v_mov_b32_e32 v211, v210
	v_mov_b32_e32 v212, v210
	v_mov_b32_e32 v213, v210
	s_waitcnt lgkmcnt(6)
	s_nop 1
	v_mfma_scale_f32_16x16x128_f8f6f4 v[84:87], v[84:91], v[8:15], v[210:213], v178, v177 op_sel_hi:[0,0,0]
	ds_read_b64 v[148:149], v207 offset:0
	ds_read_b64 v[146:147], v207 offset:32
	ds_read_b64 v[144:145], v207 offset:0x500
	ds_read_b64 v[142:143], v207 offset:0x520
	ds_read_b64 v[140:141], v207 offset:0xa00
	ds_read_b64 v[136:137], v207 offset:0xa20
	ds_read_b64 v[138:139], v207 offset:0xf00
	ds_read_b64 v[134:135], v207 offset:0xf20
	s_waitcnt lgkmcnt(12)
	v_mfma_scale_f32_16x16x128_f8f6f4 v[88:91], v[92:99], v[8:15], v[210:213], v178, v177 op_sel_hi:[0,0,0]
	s_waitcnt lgkmcnt(10)
	v_mfma_scale_f32_16x16x128_f8f6f4 v[92:95], v[118:125], v[8:15], v[210:213], v178, v177 op_sel_hi:[0,0,0]
	s_waitcnt lgkmcnt(8)
	v_mfma_scale_f32_16x16x128_f8f6f4 v[96:99], v[126:133], v[8:15], v[210:213], v178, v177 op_sel_hi:[0,0,0]
	ds_read_b64 v[132:133], v207 offset:0x1400
	ds_read_b64 v[130:131], v207 offset:0x1420
	ds_read_b64 v[128:129], v207 offset:0x1900
	ds_read_b64 v[126:127], v207 offset:0x1920
	ds_read_b64 v[124:125], v207 offset:0x1e00
	ds_read_b64 v[120:121], v207 offset:0x1e20
	ds_read_b64 v[118:119], v207 offset:0x2300
	ds_read_b64 v[122:123], v207 offset:0x2320
	s_and_b64 vcc, exec, s[12:13]
	s_cbranch_vccnz .LBB0_1812
	v_add_u32_e32 v114, s44, v155
	v_sub_u32_e32 v116, v195, v114
	v_cmp_gt_u32_e32 vcc, 2.0, v116
	v_sub_u32_e32 v116, v114, v195
	s_nop 2
	v_cndmask_b32_e32 v84, v181, v84, vcc
	v_cmp_lt_u32_e32 vcc, s91, v116
	v_sub_u32_e32 v116, v196, v114
	s_nop 0
	v_cndmask_b32_e32 v85, v181, v85, vcc
	v_cmp_gt_u32_e32 vcc, 2.0, v116
	v_sub_u32_e32 v116, v197, v114
	s_nop 0
	v_cndmask_b32_e32 v86, v181, v86, vcc
	v_cmp_gt_u32_e32 vcc, 2.0, v116
	v_sub_u32_e32 v116, s71, v114
	s_nop 0
	v_cndmask_b32_e32 v87, v181, v87, vcc
	v_cmp_gt_u32_e32 vcc, 2.0, v116
	v_sub_u32_e32 v116, v198, v114
	s_nop 0
	v_cndmask_b32_e32 v88, v181, v88, vcc
	v_cmp_gt_u32_e32 vcc, 2.0, v116
	v_sub_u32_e32 v116, v199, v114
	s_nop 0
	v_cndmask_b32_e32 v89, v181, v89, vcc
	v_cmp_gt_u32_e32 vcc, 2.0, v116
	v_sub_u32_e32 v116, v200, v114
	s_nop 0
	v_cndmask_b32_e32 v90, v181, v90, vcc
	v_cmp_gt_u32_e32 vcc, 2.0, v116
	v_sub_u32_e32 v116, s72, v114
	s_nop 0
	v_cndmask_b32_e32 v91, v181, v91, vcc
	v_cmp_gt_u32_e32 vcc, 2.0, v116
	v_sub_u32_e32 v116, v201, v114
	s_nop 0
	v_cndmask_b32_e32 v92, v181, v92, vcc
	v_cmp_gt_u32_e32 vcc, 2.0, v116
	v_sub_u32_e32 v116, v202, v114
	s_nop 0
	v_cndmask_b32_e32 v93, v181, v93, vcc
	v_cmp_gt_u32_e32 vcc, 2.0, v116
	v_sub_u32_e32 v116, v203, v114
	s_nop 0
	v_cndmask_b32_e32 v94, v181, v94, vcc
	v_cmp_gt_u32_e32 vcc, 2.0, v116
	v_sub_u32_e32 v116, s73, v114
	s_nop 0
	v_cndmask_b32_e32 v95, v181, v95, vcc
	v_cmp_gt_u32_e32 vcc, 2.0, v116
	v_sub_u32_e32 v116, v204, v114
	s_nop 0
	v_cndmask_b32_e32 v96, v181, v96, vcc
	v_cmp_gt_u32_e32 vcc, 2.0, v116
	v_sub_u32_e32 v116, v205, v114
	v_sub_u32_e32 v114, v206, v114
	v_cndmask_b32_e32 v97, v181, v97, vcc
	v_cmp_gt_u32_e32 vcc, 2.0, v116
	s_nop 1
	v_cndmask_b32_e32 v98, v181, v98, vcc
	v_cmp_gt_u32_e32 vcc, 2.0, v114
	s_nop 1
	v_cndmask_b32_e32 v99, v181, v99, vcc
